# baseline (speedup 1.0000x reference)
.Lscan_loop:
	v_exp_f32_e32 v98, v98
	v_exp_f32_e32 v99, v99
	v_mfma_f32_16x16x32_f16 v[80:83], v[72:75], v[24:27], v[80:83]
	ds_read_b128 v[60:63], v92 offset:34816
	ds_bpermute_b32 v90, v87, v85
	v_exp_f32_e32 v100, v100
	v_exp_f32_e32 v101, v101
	v_mfma_f32_32x32x16_f16 v[114:129], v[32:35], v[28:31], 0
	ds_read_u16 v32, v9 offset:64
	ds_read_b128 v[64:67], v92 offset:35840
	v_fmac_f32_e32 v132, v98, v195
	v_exp_f32_e32 v102, v102
	v_fmac_f32_e32 v133, v99, v132
	v_exp_f32_e32 v103, v103
	v_fmac_f32_e32 v134, v100, v133
	v_cvt_pkrtz_f16_f32 v68, v132, v133
	v_exp_f32_e32 v104, v104
	v_fmac_f32_e32 v135, v101, v134
	v_pk_mul_f16 v68, v52, v68
	v_exp_f32_e32 v105, v105
	v_add_f32_e32 v84, v80, v81
	v_add_f32_e32 v91, v82, v83
	v_fmac_f32_e32 v136, v102, v135
	v_add_f32_e32 v84, v84, v91
	v_cvt_pkrtz_f16_f32 v69, v134, v135
	v_mfma_f32_32x32x16_f16 v[148:163], v[36:39], v[44:47], 0
	ds_read_b128 v[44:47], v92 offset:4096
	ds_bpermute_b32 v89, v86, v84
	v_exp_f32_e32 v106, v106
	v_fmac_f32_e32 v137, v103, v136
	v_pk_mul_f16 v69, v53, v69
	v_exp_f32_e32 v107, v107
	v_fmac_f32_e32 v138, v104, v137
	v_cvt_pkrtz_f16_f32 v70, v136, v137
	v_exp_f32_e32 v108, v108
	v_fmac_f32_e32 v139, v105, v138
	v_pk_mul_f16 v70, v54, v70
	v_exp_f32_e32 v109, v109
	v_mfma_f32_32x32x16_f16 v[180:195], v[36:39], v[48:51], 0
	ds_read_b128 v[36:39], v11 offset:512
	ds_read_b128 v[48:51], v92 offset:5120
	v_cvt_pkrtz_f16_f32 v71, v138, v139
	v_fmac_f32_e32 v172, v106, v139
	v_pk_mul_f16 v71, v55, v71
	v_exp_f32_e32 v110, v110
	v_fmac_f32_e32 v173, v107, v172
	v_mfma_f32_16x16x32_f16 v[76:79], v[68:71], v[20:23], 0
	v_cvt_pkrtz_f16_f32 v72, v172, v173
	v_exp_f32_e32 v111, v111
	v_fmac_f32_e32 v174, v108, v173
	v_pk_mul_f16 v72, v56, v72
	v_fmac_f32_e32 v175, v109, v174
	v_exp_f32_e32 v112, v112
	v_cvt_pkrtz_f16_f32 v73, v174, v175
	v_fmac_f32_e32 v176, v110, v175
	v_pk_mul_f16 v73, v57, v73
	v_fmac_f32_e32 v177, v111, v176
	v_exp_f32_e32 v113, v113
	v_cvt_pkrtz_f16_f32 v74, v176, v177
	v_fmac_f32_e32 v178, v112, v177
	v_pk_mul_f16 v74, v58, v74
	s_waitcnt lgkmcnt(0)
	v_add_f32_e32 v202, v85, v90
	v_fmac_f32_e32 v179, v113, v178
	v_add_f32_e32 v88, v84, v89
	v_cvt_pkrtz_f16_f32 v75, v178, v179
	v_pk_mul_f16 v75, v59, v75
	v_exp_f32_e32 v114, v114
	v_exp_f32_e32 v115, v115
	v_mfma_f32_16x16x32_f16 v[76:79], v[72:75], v[24:27], v[76:79]
	ds_read_b128 v[52:55], v92 offset:36864
	ds_bpermute_b32 v90, v87, v88
	v_exp_f32_e32 v116, v116
	v_exp_f32_e32 v117, v117
	v_mfma_f32_32x32x16_f16 v[98:113], v[32:35], v[28:31], 0
	ds_read_u16 v32, v9 offset:96
	ds_read_b128 v[56:59], v92 offset:37888
	v_fmac_f32_e32 v148, v114, v179
	v_exp_f32_e32 v118, v118
	v_fmac_f32_e32 v149, v115, v148
	v_exp_f32_e32 v119, v119
	v_fmac_f32_e32 v150, v116, v149
	v_cvt_pkrtz_f16_f32 v68, v148, v149
	v_exp_f32_e32 v120, v120
	v_fmac_f32_e32 v151, v117, v150
	v_pk_mul_f16 v68, v60, v68
	v_exp_f32_e32 v121, v121
	v_add_f32_e32 v84, v76, v77
	v_add_f32_e32 v91, v78, v79
	v_fmac_f32_e32 v152, v118, v151
	v_add_f32_e32 v84, v84, v91
	v_cvt_pkrtz_f16_f32 v69, v150, v151
	v_mfma_f32_32x32x16_f16 v[132:147], v[36:39], v[44:47], 0
	ds_read_b128 v[44:47], v92 offset:6144
	ds_bpermute_b32 v89, v86, v84
	v_exp_f32_e32 v122, v122
	v_fmac_f32_e32 v153, v119, v152
	v_pk_mul_f16 v69, v61, v69
	v_exp_f32_e32 v123, v123
	v_fmac_f32_e32 v154, v120, v153
	v_cvt_pkrtz_f16_f32 v70, v152, v153
	v_exp_f32_e32 v124, v124
	v_fmac_f32_e32 v155, v121, v154
	v_pk_mul_f16 v70, v62, v70
	v_exp_f32_e32 v125, v125
	v_mfma_f32_32x32x16_f16 v[164:179], v[36:39], v[48:51], 0
	ds_read_b128 v[36:39], v11 offset:768
	ds_read_b128 v[48:51], v92 offset:7168
	v_cvt_pkrtz_f16_f32 v71, v154, v155
	v_fmac_f32_e32 v188, v122, v155
	v_pk_mul_f16 v71, v63, v71
	v_exp_f32_e32 v126, v126
	v_fmac_f32_e32 v189, v123, v188
	v_mfma_f32_16x16x32_f16 v[80:83], v[68:71], v[20:23], 0
	v_cvt_pkrtz_f16_f32 v72, v188, v189
	v_exp_f32_e32 v127, v127
	v_fmac_f32_e32 v190, v124, v189
	v_pk_mul_f16 v72, v64, v72
	v_fmac_f32_e32 v191, v125, v190
	v_exp_f32_e32 v128, v128
	v_cvt_pkrtz_f16_f32 v73, v190, v191
	v_fmac_f32_e32 v192, v126, v191
	v_pk_mul_f16 v73, v65, v73
	v_fmac_f32_e32 v193, v127, v192
	v_exp_f32_e32 v129, v129
	v_cvt_pkrtz_f16_f32 v74, v192, v193
	v_fmac_f32_e32 v194, v128, v193
	v_pk_mul_f16 v74, v66, v74
	s_waitcnt lgkmcnt(0)
	v_add_f32_e32 v203, v88, v90
	v_fmac_f32_e32 v195, v129, v194
	v_add_f32_e32 v85, v84, v89
	v_cvt_pkrtz_f16_f32 v75, v194, v195
	v_pk_mul_f16 v75, v67, v75
	v_exp_f32_e32 v98, v98
	v_exp_f32_e32 v99, v99
	v_mfma_f32_16x16x32_f16 v[80:83], v[72:75], v[24:27], v[80:83]
	ds_read_b128 v[60:63], v92 offset:38912
	ds_bpermute_b32 v90, v87, v85
	v_exp_f32_e32 v100, v100
	v_exp_f32_e32 v101, v101
	v_mfma_f32_32x32x16_f16 v[114:129], v[32:35], v[28:31], 0
	ds_read_u16 v32, v9 offset:128
	ds_read_b128 v[64:67], v92 offset:39936
	v_fmac_f32_e32 v132, v98, v195
	v_exp_f32_e32 v102, v102
	v_fmac_f32_e32 v133, v99, v132
	v_exp_f32_e32 v103, v103
	v_fmac_f32_e32 v134, v100, v133
	v_cvt_pkrtz_f16_f32 v68, v132, v133
	v_exp_f32_e32 v104, v104
	v_fmac_f32_e32 v135, v101, v134
	v_pk_mul_f16 v68, v52, v68
	v_exp_f32_e32 v105, v105
	v_add_f32_e32 v84, v80, v81
	v_add_f32_e32 v91, v82, v83
	v_fmac_f32_e32 v136, v102, v135
	v_add_f32_e32 v84, v84, v91
	v_cvt_pkrtz_f16_f32 v69, v134, v135
	v_mfma_f32_32x32x16_f16 v[148:163], v[36:39], v[44:47], 0
	ds_read_b128 v[44:47], v92 offset:8192
	ds_bpermute_b32 v89, v86, v84
	v_exp_f32_e32 v106, v106
	v_fmac_f32_e32 v137, v103, v136
	v_pk_mul_f16 v69, v53, v69
	v_exp_f32_e32 v107, v107
	v_fmac_f32_e32 v138, v104, v137
	v_cvt_pkrtz_f16_f32 v70, v136, v137
	v_exp_f32_e32 v108, v108
	v_fmac_f32_e32 v139, v105, v138
	v_pk_mul_f16 v70, v54, v70
	v_exp_f32_e32 v109, v109
	v_mfma_f32_32x32x16_f16 v[180:195], v[36:39], v[48:51], 0
	ds_read_b128 v[36:39], v11 offset:1024
	ds_read_b128 v[48:51], v92 offset:9216
	v_cvt_pkrtz_f16_f32 v71, v138, v139
	v_fmac_f32_e32 v172, v106, v139
	v_pk_mul_f16 v71, v55, v71
	v_exp_f32_e32 v110, v110
	v_fmac_f32_e32 v173, v107, v172
	v_mfma_f32_16x16x32_f16 v[76:79], v[68:71], v[20:23], 0
	v_cvt_pkrtz_f16_f32 v72, v172, v173
	v_exp_f32_e32 v111, v111
	v_fmac_f32_e32 v174, v108, v173
	v_pk_mul_f16 v72, v56, v72
	v_fmac_f32_e32 v175, v109, v174
	v_exp_f32_e32 v112, v112
	v_cvt_pkrtz_f16_f32 v73, v174, v175
	v_fmac_f32_e32 v176, v110, v175
	v_pk_mul_f16 v73, v57, v73
	v_fmac_f32_e32 v177, v111, v176
	v_exp_f32_e32 v113, v113
	v_cvt_pkrtz_f16_f32 v74, v176, v177
	v_fmac_f32_e32 v178, v112, v177
	v_pk_mul_f16 v74, v58, v74
	s_waitcnt lgkmcnt(0)
	v_add_f32_e32 v196, v85, v90
	v_fmac_f32_e32 v179, v113, v178
	v_add_f32_e32 v88, v84, v89
	v_cvt_pkrtz_f16_f32 v75, v178, v179
	v_pk_mul_f16 v75, v59, v75
	v_exp_f32_e32 v114, v114
	v_exp_f32_e32 v115, v115
	v_mfma_f32_16x16x32_f16 v[76:79], v[72:75], v[24:27], v[76:79]
	ds_read_b128 v[52:55], v92 offset:40960
	ds_bpermute_b32 v90, v87, v88
	v_exp_f32_e32 v116, v116
	v_exp_f32_e32 v117, v117
	v_mfma_f32_32x32x16_f16 v[98:113], v[32:35], v[28:31], 0
	ds_read_u16 v32, v9 offset:160
	ds_read_b128 v[56:59], v92 offset:41984
	v_fmac_f32_e32 v148, v114, v179
	v_exp_f32_e32 v118, v118
	v_fmac_f32_e32 v149, v115, v148
	v_exp_f32_e32 v119, v119
	v_fmac_f32_e32 v150, v116, v149
	v_cvt_pkrtz_f16_f32 v68, v148, v149
	v_exp_f32_e32 v120, v120
	v_fmac_f32_e32 v151, v117, v150
	v_pk_mul_f16 v68, v60, v68
	v_exp_f32_e32 v121, v121
	v_add_f32_e32 v84, v76, v77
	v_add_f32_e32 v91, v78, v79
	v_fmac_f32_e32 v152, v118, v151
	v_add_f32_e32 v84, v84, v91
	v_cvt_pkrtz_f16_f32 v69, v150, v151
	v_mfma_f32_32x32x16_f16 v[132:147], v[36:39], v[44:47], 0
	ds_read_b128 v[44:47], v92 offset:10240
	ds_bpermute_b32 v89, v86, v84
	v_exp_f32_e32 v122, v122
	v_fmac_f32_e32 v153, v119, v152
	v_pk_mul_f16 v69, v61, v69
	v_exp_f32_e32 v123, v123
	v_fmac_f32_e32 v154, v120, v153
	v_cvt_pkrtz_f16_f32 v70, v152, v153
	v_exp_f32_e32 v124, v124
	v_fmac_f32_e32 v155, v121, v154
	v_pk_mul_f16 v70, v62, v70
	v_exp_f32_e32 v125, v125
	v_mfma_f32_32x32x16_f16 v[164:179], v[36:39], v[48:51], 0
	ds_read_b128 v[36:39], v11 offset:1280
	ds_read_b128 v[48:51], v92 offset:11264
	v_cvt_pkrtz_f16_f32 v71, v154, v155
	v_fmac_f32_e32 v188, v122, v155
	v_pk_mul_f16 v71, v63, v71
	v_exp_f32_e32 v126, v126
	v_fmac_f32_e32 v189, v123, v188
	v_mfma_f32_16x16x32_f16 v[80:83], v[68:71], v[20:23], 0
	v_cvt_pkrtz_f16_f32 v72, v188, v189
	v_exp_f32_e32 v127, v127
	v_fmac_f32_e32 v190, v124, v189
	v_pk_mul_f16 v72, v64, v72
	v_fmac_f32_e32 v191, v125, v190
	v_exp_f32_e32 v128, v128
	v_cvt_pkrtz_f16_f32 v73, v190, v191
	v_fmac_f32_e32 v192, v126, v191
	v_pk_mul_f16 v73, v65, v73
	v_fmac_f32_e32 v193, v127, v192
	v_exp_f32_e32 v129, v129
	v_cvt_pkrtz_f16_f32 v74, v192, v193
	v_fmac_f32_e32 v194, v128, v193
	v_pk_mul_f16 v74, v66, v74
	s_waitcnt lgkmcnt(0)
	v_add_f32_e32 v197, v88, v90
	v_fmac_f32_e32 v195, v129, v194
	v_add_f32_e32 v85, v84, v89
	v_cvt_pkrtz_f16_f32 v75, v194, v195
	v_pk_mul_f16 v75, v67, v75
	v_exp_f32_e32 v98, v98
	v_exp_f32_e32 v99, v99
	v_mfma_f32_16x16x32_f16 v[80:83], v[72:75], v[24:27], v[80:83]
	ds_read_b128 v[60:63], v92 offset:43008
	ds_bpermute_b32 v90, v87, v85
	v_exp_f32_e32 v100, v100
	v_exp_f32_e32 v101, v101
	v_mfma_f32_32x32x16_f16 v[114:129], v[32:35], v[28:31], 0
	ds_read_u16 v32, v9 offset:192
	ds_read_b128 v[64:67], v92 offset:44032
	v_fmac_f32_e32 v132, v98, v195
	v_exp_f32_e32 v102, v102
	v_fmac_f32_e32 v133, v99, v132
	v_exp_f32_e32 v103, v103
	v_fmac_f32_e32 v134, v100, v133
	v_cvt_pkrtz_f16_f32 v68, v132, v133
	v_exp_f32_e32 v104, v104
	v_fmac_f32_e32 v135, v101, v134
	v_pk_mul_f16 v68, v52, v68
	v_exp_f32_e32 v105, v105
	v_add_f32_e32 v84, v80, v81
	v_add_f32_e32 v91, v82, v83
	v_fmac_f32_e32 v136, v102, v135
	v_add_f32_e32 v84, v84, v91
	v_cvt_pkrtz_f16_f32 v69, v134, v135
	v_mfma_f32_32x32x16_f16 v[148:163], v[36:39], v[44:47], 0
	ds_read_b128 v[44:47], v92 offset:12288
	ds_bpermute_b32 v89, v86, v84
	v_exp_f32_e32 v106, v106
	v_fmac_f32_e32 v137, v103, v136
	v_pk_mul_f16 v69, v53, v69
	v_exp_f32_e32 v107, v107
	v_fmac_f32_e32 v138, v104, v137
	v_cvt_pkrtz_f16_f32 v70, v136, v137
	v_exp_f32_e32 v108, v108
	v_fmac_f32_e32 v139, v105, v138
	v_pk_mul_f16 v70, v54, v70
	v_exp_f32_e32 v109, v109
	v_mfma_f32_32x32x16_f16 v[180:195], v[36:39], v[48:51], 0
	ds_read_b128 v[36:39], v11 offset:1536
	ds_read_b128 v[48:51], v92 offset:13312
	v_cvt_pkrtz_f16_f32 v71, v138, v139
	v_fmac_f32_e32 v172, v106, v139
	v_pk_mul_f16 v71, v55, v71
	v_exp_f32_e32 v110, v110
	v_fmac_f32_e32 v173, v107, v172
	v_mfma_f32_16x16x32_f16 v[76:79], v[68:71], v[20:23], 0
	v_cvt_pkrtz_f16_f32 v72, v172, v173
	v_exp_f32_e32 v111, v111
	v_fmac_f32_e32 v174, v108, v173
	v_pk_mul_f16 v72, v56, v72
	v_fmac_f32_e32 v175, v109, v174
	v_exp_f32_e32 v112, v112
	v_cvt_pkrtz_f16_f32 v73, v174, v175
	v_fmac_f32_e32 v176, v110, v175
	v_pk_mul_f16 v73, v57, v73
	v_fmac_f32_e32 v177, v111, v176
	v_exp_f32_e32 v113, v113
	v_cvt_pkrtz_f16_f32 v74, v176, v177
	v_fmac_f32_e32 v178, v112, v177
	v_pk_mul_f16 v74, v58, v74
	s_waitcnt lgkmcnt(0)
	v_add_f32_e32 v198, v85, v90
	v_fmac_f32_e32 v179, v113, v178
	v_add_f32_e32 v88, v84, v89
	v_cvt_pkrtz_f16_f32 v75, v178, v179
	v_pk_mul_f16 v75, v59, v75
	v_exp_f32_e32 v114, v114
	v_exp_f32_e32 v115, v115
	v_mfma_f32_16x16x32_f16 v[76:79], v[72:75], v[24:27], v[76:79]
	ds_read_b128 v[52:55], v92 offset:45056
	ds_bpermute_b32 v90, v87, v88
	s_waitcnt vmcnt(0)
	ds_write_b16 v94, v18
	ds_write_b16 v94, v19 offset:1024
	ds_read_b128 v[204:207], v92 offset:47104
	ds_read_b128 v[208:211], v92 offset:48128
	v_exp_f32_e32 v116, v116
	v_exp_f32_e32 v117, v117
	v_mfma_f32_32x32x16_f16 v[98:113], v[32:35], v[28:31], 0
	ds_read_u16 v32, v9 offset:224
	ds_read_b128 v[56:59], v92 offset:46080
	v_fmac_f32_e32 v148, v114, v179
	v_exp_f32_e32 v118, v118
	v_fmac_f32_e32 v149, v115, v148
	v_exp_f32_e32 v119, v119
	v_fmac_f32_e32 v150, v116, v149
	v_cvt_pkrtz_f16_f32 v68, v148, v149
	v_exp_f32_e32 v120, v120
	v_fmac_f32_e32 v151, v117, v150
	v_pk_mul_f16 v68, v60, v68
	v_exp_f32_e32 v121, v121
	v_add_f32_e32 v84, v76, v77
	v_add_f32_e32 v91, v78, v79
	v_fmac_f32_e32 v152, v118, v151
	v_add_f32_e32 v84, v84, v91
	v_cvt_pkrtz_f16_f32 v69, v150, v151
	v_mfma_f32_32x32x16_f16 v[132:147], v[36:39], v[44:47], 0
	ds_read_b128 v[44:47], v92 offset:14336
	ds_bpermute_b32 v89, v86, v84
	v_exp_f32_e32 v122, v122
	v_fmac_f32_e32 v153, v119, v152
	v_pk_mul_f16 v69, v61, v69
	v_exp_f32_e32 v123, v123
	v_fmac_f32_e32 v154, v120, v153
	v_cvt_pkrtz_f16_f32 v70, v152, v153
	v_exp_f32_e32 v124, v124
	v_fmac_f32_e32 v155, v121, v154
	v_pk_mul_f16 v70, v62, v70
	v_exp_f32_e32 v125, v125
	v_mfma_f32_32x32x16_f16 v[164:179], v[36:39], v[48:51], 0
	ds_read_b128 v[36:39], v11 offset:1792
	ds_read_b128 v[48:51], v92 offset:15360
	v_cvt_pkrtz_f16_f32 v71, v154, v155
	v_fmac_f32_e32 v188, v122, v155
	v_pk_mul_f16 v71, v63, v71
	v_exp_f32_e32 v126, v126
	v_fmac_f32_e32 v189, v123, v188
	v_mfma_f32_16x16x32_f16 v[80:83], v[68:71], v[20:23], 0
	v_cvt_pkrtz_f16_f32 v72, v188, v189
	v_exp_f32_e32 v127, v127
	v_fmac_f32_e32 v190, v124, v189
	v_pk_mul_f16 v72, v64, v72
	v_fmac_f32_e32 v191, v125, v190
	v_exp_f32_e32 v128, v128
	v_cvt_pkrtz_f16_f32 v73, v190, v191
	v_fmac_f32_e32 v192, v126, v191
	v_pk_mul_f16 v73, v65, v73
	v_fmac_f32_e32 v193, v127, v192
	v_exp_f32_e32 v129, v129
	v_cvt_pkrtz_f16_f32 v74, v192, v193
	v_fmac_f32_e32 v194, v128, v193
	v_pk_mul_f16 v74, v66, v74
	s_waitcnt lgkmcnt(0)
	v_add_f32_e32 v199, v88, v90
	v_fmac_f32_e32 v195, v129, v194
	v_add_f32_e32 v85, v84, v89
	v_cvt_pkrtz_f16_f32 v75, v194, v195
	v_pk_mul_f16 v75, v67, v75
	v_exp_f32_e32 v98, v98
	v_exp_f32_e32 v99, v99
	v_mfma_f32_16x16x32_f16 v[80:83], v[72:75], v[24:27], v[80:83]
	s_waitcnt lgkmcnt(0)
	s_barrier
	ds_bpermute_b32 v90, v87, v85
	v_exp_f32_e32 v100, v100
	v_exp_f32_e32 v101, v101
	v_mfma_f32_32x32x16_f16 v[114:129], v[32:35], v[28:31], 0
	s_mov_b32 m0, s32
	ds_read_u16 v32, v10 offset:0
	global_load_lds_dwordx4 v2, s[20:21]
	v_fmac_f32_e32 v132, v98, v195
	v_exp_f32_e32 v102, v102
	v_fmac_f32_e32 v133, v99, v132
	v_exp_f32_e32 v103, v103
	v_fmac_f32_e32 v134, v100, v133
	v_cvt_pkrtz_f16_f32 v68, v132, v133
	v_exp_f32_e32 v104, v104
	v_fmac_f32_e32 v135, v101, v134
	v_pk_mul_f16 v68, v52, v68
	v_exp_f32_e32 v105, v105
	v_add_f32_e32 v84, v80, v81
	v_add_f32_e32 v91, v82, v83
	v_fmac_f32_e32 v136, v102, v135
	v_add_f32_e32 v84, v84, v91
	v_cvt_pkrtz_f16_f32 v69, v134, v135
	v_mfma_f32_32x32x16_f16 v[148:163], v[36:39], v[44:47], 0
	ds_read_b128 v[44:47], v93 offset:0
	ds_bpermute_b32 v89, v86, v84
	s_add_i32 m0, s32, 32768
	s_nop 0
	global_load_lds_dwordx4 v2, s[22:23]
	v_exp_f32_e32 v106, v106
	v_fmac_f32_e32 v137, v103, v136
	v_pk_mul_f16 v69, v53, v69
	v_exp_f32_e32 v107, v107
	v_fmac_f32_e32 v138, v104, v137
	v_cvt_pkrtz_f16_f32 v70, v136, v137
	v_exp_f32_e32 v108, v108
	v_fmac_f32_e32 v139, v105, v138
	v_pk_mul_f16 v70, v54, v70
	v_exp_f32_e32 v109, v109
	v_mfma_f32_32x32x16_f16 v[180:195], v[36:39], v[48:51], 0
	ds_read_b128 v[36:39], v13 offset:0
	s_mov_b32 m0, s33
	ds_read_b128 v[48:51], v93 offset:1024
	global_load_lds_dwordx4 v3, s[20:21]
	v_cvt_pkrtz_f16_f32 v71, v138, v139
	v_fmac_f32_e32 v172, v106, v139
	v_pk_mul_f16 v71, v55, v71
	v_exp_f32_e32 v110, v110
	v_fmac_f32_e32 v173, v107, v172
	v_mfma_f32_16x16x32_f16 v[76:79], v[68:71], v[20:23], 0
	s_add_i32 m0, s33, 32768
	s_nop 0
	global_load_lds_dwordx4 v3, s[22:23]
	v_cvt_pkrtz_f16_f32 v72, v172, v173
	v_exp_f32_e32 v111, v111
	v_fmac_f32_e32 v174, v108, v173
	v_pk_mul_f16 v72, v56, v72
	v_fmac_f32_e32 v175, v109, v174
	v_exp_f32_e32 v112, v112
	v_cvt_pkrtz_f16_f32 v73, v174, v175
	v_fmac_f32_e32 v176, v110, v175
	v_pk_mul_f16 v73, v57, v73
	v_fmac_f32_e32 v177, v111, v176
	v_exp_f32_e32 v113, v113
	v_cvt_pkrtz_f16_f32 v74, v176, v177
	v_fmac_f32_e32 v178, v112, v177
	v_pk_mul_f16 v74, v58, v74
	s_waitcnt lgkmcnt(0)
	v_add_f32_e32 v200, v85, v90
	v_fmac_f32_e32 v179, v113, v178
	v_add_f32_e32 v88, v84, v89
	v_cvt_pkrtz_f16_f32 v75, v178, v179
	v_pk_mul_f16 v75, v59, v75
	v_exp_f32_e32 v114, v114
	v_exp_f32_e32 v115, v115
	v_mfma_f32_16x16x32_f16 v[76:79], v[72:75], v[24:27], v[76:79]
	s_mov_b32 m0, s34
	ds_read_b128 v[52:55], v93 offset:32768
	global_load_lds_dwordx4 v4, s[20:21]
	ds_bpermute_b32 v90, v87, v88
	v_exp_f32_e32 v116, v116
	v_exp_f32_e32 v117, v117
	v_mfma_f32_32x32x16_f16 v[98:113], v[32:35], v[28:31], 0
	ds_read_u16 v32, v10 offset:32
	s_add_i32 m0, s34, 32768
	ds_read_b128 v[56:59], v93 offset:33792
	global_load_lds_dwordx4 v4, s[22:23]
	v_fmac_f32_e32 v148, v114, v179
	v_exp_f32_e32 v118, v118
	v_fmac_f32_e32 v149, v115, v148
	v_exp_f32_e32 v119, v119
	v_fmac_f32_e32 v150, v116, v149
	v_cvt_pkrtz_f16_f32 v68, v148, v149
	v_exp_f32_e32 v120, v120
	v_fmac_f32_e32 v151, v117, v150
	v_pk_mul_f16 v68, v204, v68
	v_exp_f32_e32 v121, v121
	v_add_f32_e32 v84, v76, v77
	v_add_f32_e32 v91, v78, v79
	v_fmac_f32_e32 v152, v118, v151
	v_add_f32_e32 v84, v84, v91
	v_cvt_pkrtz_f16_f32 v69, v150, v151
	v_mfma_f32_32x32x16_f16 v[132:147], v[36:39], v[44:47], 0
	ds_read_b128 v[44:47], v93 offset:2048
	ds_bpermute_b32 v89, v86, v84
	s_cmp_eq_u32 s40, 0
	s_cselect_b64 s[56:57], 0, s[42:43]
	s_and_saveexec_b64 s[44:45], s[56:57]
	global_store_dword v[16:17], v201, off offset:-192 sc1
	global_store_dword v[16:17], v202, off offset:-128 sc1
	global_store_dword v[16:17], v203, off offset:-64 sc1
	s_and_b64 exec, s[44:45], s[42:43]
	global_store_dword v[16:17], v196, off sc1
	global_store_dword v[16:17], v197, off offset:64 sc1
	global_store_dword v[16:17], v198, off offset:128 sc1
	global_store_dword v[16:17], v199, off offset:192 sc1
	global_store_dword v[16:17], v200, off offset:256 sc1
	s_mov_b64 exec, s[44:45]
	v_exp_f32_e32 v122, v122
	v_fmac_f32_e32 v153, v119, v152
	v_pk_mul_f16 v69, v205, v69
	v_exp_f32_e32 v123, v123
	v_fmac_f32_e32 v154, v120, v153
	v_cvt_pkrtz_f16_f32 v70, v152, v153
	v_exp_f32_e32 v124, v124
	v_fmac_f32_e32 v155, v121, v154
	v_pk_mul_f16 v70, v206, v70
	v_exp_f32_e32 v125, v125
	v_mfma_f32_32x32x16_f16 v[164:179], v[36:39], v[48:51], 0
	ds_read_b128 v[36:39], v13 offset:256
	s_mov_b32 m0, s35
	ds_read_b128 v[48:51], v93 offset:3072
	global_load_lds_dwordx4 v5, s[20:21]
	s_add_i32 m0, s35, 32768
	s_nop 0
	global_load_lds_dwordx4 v5, s[22:23]
	v_cvt_pkrtz_f16_f32 v71, v154, v155
	v_fmac_f32_e32 v188, v122, v155
	v_pk_mul_f16 v71, v207, v71
	v_exp_f32_e32 v126, v126
	v_fmac_f32_e32 v189, v123, v188
	v_mfma_f32_16x16x32_f16 v[80:83], v[68:71], v[20:23], 0
	s_mov_b32 m0, s29
	s_nop 0
	global_load_lds_dword v6, s[24:25]
	global_load_ushort v18, v7, s[26:27]
	global_load_ushort v19, v7, s[26:27] offset:128
	v_cvt_pkrtz_f16_f32 v72, v188, v189
	v_exp_f32_e32 v127, v127
	v_fmac_f32_e32 v190, v124, v189
	v_pk_mul_f16 v72, v208, v72
	v_fmac_f32_e32 v191, v125, v190
	v_exp_f32_e32 v128, v128
	v_cvt_pkrtz_f16_f32 v73, v190, v191
	v_fmac_f32_e32 v192, v126, v191
	v_pk_mul_f16 v73, v209, v73
	v_fmac_f32_e32 v193, v127, v192
	v_exp_f32_e32 v129, v129
	v_cvt_pkrtz_f16_f32 v74, v192, v193
	v_fmac_f32_e32 v194, v128, v193
	v_pk_mul_f16 v74, v210, v74
	s_waitcnt lgkmcnt(0)
	v_add_f32_e32 v201, v88, v90
	v_fmac_f32_e32 v195, v129, v194
	v_add_f32_e32 v85, v84, v89
	v_cvt_pkrtz_f16_f32 v75, v194, v195
	s_cmp_lt_u32 s40, 29
	s_cselect_b32 s58, 0x4000, 0
	s_cselect_b32 s59, 0x100, 0
	s_add_u32 s20, s20, s58
	s_addc_u32 s21, s21, 0
	s_add_u32 s22, s22, s58
	s_addc_u32 s23, s23, 0
	s_add_u32 s24, s24, s59
	s_addc_u32 s25, s25, 0
	s_add_u32 s26, s26, s59
	s_addc_u32 s27, s27, 0
	v_pk_mul_f16 v75, v211, v75
	v_lshl_add_u64 v[16:17], v[16:17], 0, s[46:47]
	v_swap_b32 v92, v93
	v_swap_b32 v9, v10
	v_swap_b32 v11, v13
	v_swap_b32 v8, v94
	s_xor_b32 s32, s32, 0x4000
	s_xor_b32 s33, s33, 0x4000
	s_xor_b32 s34, s34, 0x4000
	s_xor_b32 s35, s35, 0x4000
	s_xor_b32 s29, s29, 0x100
	s_add_u32 s40, s40, 1
	s_cmp_lt_u32 s40, 32
	s_cbranch_scc1 .Lscan_loop
	s_nop 1
	v_mfma_f32_16x16x32_f16 v[80:83], v[72:75], v[24:27], v[80:83]
	ds_bpermute_b32 v90, v87, v85
	s_nop 15
	v_add_f32_e32 v84, v80, v81
	v_add_f32_e32 v91, v82, v83
	s_nop 0
	v_add_f32_e32 v84, v84, v91
	s_waitcnt lgkmcnt(0)
	v_add_f32_e32 v202, v85, v90
	ds_bpermute_b32 v89, v86, v84
	s_waitcnt lgkmcnt(0)
	v_add_f32_e32 v88, v84, v89
	s_nop 0
	ds_bpermute_b32 v90, v87, v88
	s_waitcnt lgkmcnt(0)
	v_add_f32_e32 v203, v88, v90
	s_nop 1
	s_and_saveexec_b64 s[44:45], s[42:43]
	global_store_dword v[16:17], v201, off offset:-192 sc1
	global_store_dword v[16:17], v202, off offset:-128 sc1
	global_store_dword v[16:17], v203, off offset:-64 sc1
	s_waitcnt vmcnt(0)
	s_endpgm
